# speedup vs baseline: 1.0051x; 1.0040x over previous
.LBB2_3:
	s_add_u32 s79, s78, 4
	s_cmp_lt_i32 s77, s79
	s_cselect_b32 s79, s78, s79
	s_add_u32 s78, s78, 4
	s_lshl_b32 s79, s79, 13
	s_add_u32 s84, s80, s79
	s_addc_u32 s85, s81, 0
	s_add_u32 s86, s84, 0x1000
	s_addc_u32 s87, s85, 0
	s_add_u32 s88, s82, s79
	s_addc_u32 s89, s83, 0
	s_add_u32 s90, s88, 0x1000
	s_addc_u32 s91, s89, 0
	v_mov_b32_e32 v196, v191
	s_waitcnt vmcnt(9)
	v_mov_b64_e32 v[158:159], v[142:143]
	v_add_u32_e32 v191, 4, v196
	v_mfma_f32_32x32x16_bf16 v[52:67], v[100:103], v[68:71], 0
	v_mov_b64_e32 v[156:157], v[140:141]
	v_mov_b64_e32 v[142:143], v[138:139]
	v_cmp_lt_i32_e64 s[68:69], s77, v191
	v_mov_b64_e32 v[140:141], v[136:137]
	v_mov_b64_e32 v[138:139], v[110:111]
	v_mov_b64_e32 v[136:137], v[108:109]
	global_load_dwordx4 v[100:103], v203, s[84:85] nt
	global_load_dwordx4 v[108:111], v203, s[84:85] offset:1024 nt
	v_mfma_f32_32x32x16_bf16 v[36:51], v[132:135], v[68:71], 0
	s_waitcnt vmcnt(10)
	v_mov_b64_e32 v[194:195], v[146:147]
	v_mov_b64_e32 v[192:193], v[144:145]
	v_mov_b64_e32 v[146:147], v[118:119]
	v_mov_b64_e32 v[144:145], v[116:117]
	v_mov_b64_e32 v[174:175], v[122:123]
	v_mov_b64_e32 v[172:173], v[120:121]
	v_mfma_f32_32x32x16_bf16 v[52:67], v[136:139], v[72:75], v[52:67]
	v_mfma_f32_32x32x16_bf16 v[36:51], v[140:143], v[72:75], v[36:51]
	v_mfma_f32_32x32x16_bf16 v[52:67], v[144:147], v[76:79], v[52:67]
	global_load_dwordx4 v[116:119], v203, s[84:85] offset:2048 nt
	s_nop 0
	global_load_dwordx4 v[120:123], v203, s[84:85] offset:3072 nt
	s_nop 0
	global_load_dwordx4 v[132:135], v203, s[86:87] nt
	s_nop 0
	global_load_dwordx4 v[136:139], v203, s[86:87] offset:1024 nt
	s_nop 0
	global_load_dwordx4 v[140:143], v203, s[86:87] offset:2048 nt
	s_nop 0
	global_load_dwordx4 v[144:147], v203, s[86:87] offset:3072 nt
	global_load_dwordx4 v[148:151], v203, s[88:89] nt
	s_nop 0
	global_load_dwordx4 v[152:155], v203, s[88:89] offset:1024 nt
	v_mfma_f32_32x32x16_bf16 v[36:51], v[156:159], v[76:79], v[36:51]
	global_load_dwordx4 v[156:159], v203, s[88:89] offset:2048 nt
	global_load_dwordx4 v[168:171], v203, s[88:89] offset:3072 nt
	global_load_dwordx4 v[160:163], v203, s[90:91] nt
	s_nop 0
	global_load_dwordx4 v[164:167], v203, s[90:91] offset:1024 nt
	v_cmp_eq_u32_e32 vcc, s77, v196
	v_mfma_f32_32x32x16_bf16 v[52:67], v[172:175], v[80:83], v[52:67]
	global_load_dwordx4 v[172:175], v203, s[90:91] offset:2048 nt
	s_nop 0
	global_load_dwordx4 v[176:179], v203, s[90:91] offset:3072 nt
	v_mfma_f32_32x32x16_bf16 v[36:51], v[192:195], v[80:83], v[36:51]
	s_and_saveexec_b64 s[74:75], vcc
	s_cbranch_execz .LBB2_5
	s_nop 5
	v_cndmask_b32_e64 v34, v52, v190, s[2:3]
	s_nop 2
	v_cndmask_b32_e64 v36, v36, v190, s[4:5]
	v_cndmask_b32_e64 v53, v190, v53, s[6:7]
	v_cndmask_b32_e64 v52, v34, v52, s[6:7]
	v_cndmask_b32_e64 v37, v37, v190, s[8:9]
	v_cndmask_b32_e64 v54, v54, v190, s[10:11]
	v_cndmask_b32_e64 v38, v38, v190, s[12:13]
	v_cndmask_b32_e64 v55, v55, v190, s[14:15]
	v_cndmask_b32_e64 v39, v39, v190, s[16:17]
	v_cndmask_b32_e64 v56, v56, v190, s[18:19]
	v_cndmask_b32_e64 v40, v40, v190, s[20:21]
	v_cndmask_b32_e64 v57, v57, v190, s[22:23]
	v_cndmask_b32_e64 v41, v41, v190, s[24:25]
	v_cndmask_b32_e64 v58, v58, v190, s[26:27]
	v_cndmask_b32_e64 v42, v42, v190, s[28:29]
	v_cndmask_b32_e64 v59, v59, v190, s[30:31]
	v_cndmask_b32_e64 v43, v43, v190, s[34:35]
	v_cndmask_b32_e64 v60, v60, v190, s[36:37]
	v_cndmask_b32_e64 v44, v44, v190, s[38:39]
	v_cndmask_b32_e64 v61, v61, v190, s[40:41]
	v_cndmask_b32_e64 v45, v45, v190, s[42:43]
	v_cndmask_b32_e64 v62, v62, v190, s[44:45]
	v_cndmask_b32_e64 v46, v46, v190, s[46:47]
	v_cndmask_b32_e64 v63, v63, v190, s[48:49]
	v_cndmask_b32_e64 v47, v47, v190, s[50:51]
	v_cndmask_b32_e64 v64, v64, v190, s[52:53]
	v_cndmask_b32_e64 v48, v48, v190, s[54:55]
	v_cndmask_b32_e64 v65, v65, v190, s[56:57]
	v_cndmask_b32_e64 v49, v49, v190, s[58:59]
	v_cndmask_b32_e64 v66, v66, v190, s[60:61]
	v_cndmask_b32_e64 v50, v50, v190, s[62:63]
	v_cndmask_b32_e64 v67, v67, v190, s[64:65]
	v_cndmask_b32_e64 v51, v51, v190, s[66:67]
